# baseline (speedup 1.0000x reference)
.Lprio_done:
	s_cmp_eq_u32 s3, 3
	v_lshl_add_u32 v0, s3, 17, v217
	v_add_u32_e32 v1, 0x20000, v0
	s_cselect_b64 vcc, -1, 0
	v_cndmask_b32_e32 v0, v1, v0, vcc
	v_or_b32_e32 v0, v0, v215
	v_ashrrev_i32_e32 v1, 31, v0
	v_lshl_add_u64 v[0:1], v[0:1], 2, s[40:41]
	v_mov_b32_e32 v2, v219
	v_mov_b32_e32 v3, v218
	global_load_dword v218, v[0:1], off
	global_load_dword v219, v[0:1], off offset:256
	v_add_f32_e32 v0, v2, v3
	s_nop 1
	v_add_f32_dpp v0, v0, v0 quad_perm:[1,0,3,2] row_mask:0xf bank_mask:0xf bound_ctrl:1
	s_nop 1
	v_add_f32_dpp v0, v0, v0 quad_perm:[2,3,0,1] row_mask:0xf bank_mask:0xf bound_ctrl:1
	s_nop 1
	v_add_f32_dpp v0, v0, v0 row_half_mirror row_mask:0xf bank_mask:0xf bound_ctrl:1
	s_nop 1
	v_add_f32_dpp v0, v0, v0 row_mirror row_mask:0xf bank_mask:0xf bound_ctrl:1
	s_nop 0
	v_readlane_b32 s1, v0, 16
	v_readlane_b32 s9, v0, 48
	v_readlane_b32 s0, v0, 0
	v_readlane_b32 s8, v0, 32
	v_mov_b32_e32 v0, s1
	v_mov_b32_e32 v1, s9
	v_add_f32_e32 v0, s0, v0
	v_add_f32_e32 v1, s8, v1
	v_add_f32_e32 v0, v0, v1
	v_fma_mixlo_f16 v1, v0, s33, v3
	v_fma_mixlo_f16 v0, v0, s33, v2
	ds_write_b16 v220, v1 offset:14
	ds_write_b16 v220, v0 offset:142
	ds_write_b16 v220, v1 offset:300
	ds_write_b16 v220, v0 offset:428
	ds_read2_b32 v[2:3], v223 offset0:2 offset1:3
	ds_read2_b32 v[0:1], v223 offset1:1
	ds_read2_b32 v[4:5], v223 offset0:32 offset1:33
	ds_read2_b32 v[6:7], v223 offset0:34 offset1:35
	s_mov_b32 s8, 0
	s_mov_b32 s9, s8
	s_mov_b32 s10, s8
	s_waitcnt lgkmcnt(3)
	v_or_b32_sdwa v8, v3, s34 dst_sel:DWORD dst_unused:UNUSED_PAD src0_sel:WORD_0 src1_sel:DWORD
	v_cndmask_b32_e64 v3, v8, v3, s[4:5]
	s_mov_b32 s11, s8
	s_mov_b32 s12, s8
	s_waitcnt lgkmcnt(2)
	v_mfma_f32_32x32x16_f16 v[64:79], v[200:203], v[0:3], 0
	ds_read2_b32 v[2:3], v224 offset0:2 offset1:3
	ds_read2_b32 v[0:1], v224 offset1:1
	ds_read2_b32 v[16:17], v225 offset1:1
	ds_read2_b32 v[18:19], v225 offset0:2 offset1:3
	s_mov_b32 s13, s8
	s_mov_b32 s14, s8
	s_mov_b32 s15, s8
	s_waitcnt lgkmcnt(3)
	v_or_b32_sdwa v8, v3, s34 dst_sel:DWORD dst_unused:UNUSED_PAD src0_sel:WORD_0 src1_sel:DWORD
	s_waitcnt lgkmcnt(0)
	v_or_b32_sdwa v20, v19, s34 dst_sel:DWORD dst_unused:UNUSED_PAD src0_sel:WORD_0 src1_sel:DWORD
	v_cndmask_b32_e64 v19, v20, v19, s[4:5]
	v_cndmask_b32_e64 v3, v8, v3, s[4:5]
	s_mov_b32 s16, s8
	v_mfma_f32_32x32x16_f16 v[16:31], v[200:203], v[16:19], 0
	s_mov_b32 s17, s8
	s_mov_b32 s18, s8
	s_mov_b32 s19, s8
	s_mov_b32 s20, s8
	s_mov_b32 s21, s8
	s_mov_b32 s22, s8
	s_mov_b32 s23, s8
	v_mfma_f32_32x32x16_f16 v[48:63], v[200:203], v[0:3], 0
	v_or_b32_sdwa v0, v7, s34 dst_sel:DWORD dst_unused:UNUSED_PAD src0_sel:WORD_0 src1_sel:DWORD
	v_cndmask_b32_e64 v7, v0, v7, s[4:5]
	s_nop 1
	v_mfma_f32_32x32x16_f16 v[32:47], v[200:203], v[4:7], 0
	v_mov_b64_e32 v[0:1], s[8:9]
	v_mov_b64_e32 v[2:3], s[10:11]
	v_mov_b64_e32 v[4:5], s[12:13]
	v_mov_b64_e32 v[6:7], s[14:15]
	v_mov_b64_e32 v[8:9], s[16:17]
	v_mov_b64_e32 v[10:11], s[18:19]
	v_mov_b64_e32 v[12:13], s[20:21]
	v_mov_b64_e32 v[14:15], s[22:23]
	s_nop 15
	s_nop 3
	v_cvt_pk_f16_f32 v239, v64, v65
	v_cvt_pk_f16_f32 v240, v66, v67
	v_and_b32 v209, s35, v239
	v_and_b32 v238, s35, v240
	v_pk_fma_f16 v236, v209, s42, v227
	v_pk_fma_f16 v237, v238, s42, v227
	v_pk_fma_f16 v236, v236, v209, s43
	v_pk_fma_f16 v237, v237, v238, s43
	s_nop 0
	v_pk_mul_f16 v236, v236, v209
	v_pk_mul_f16 v237, v237, v238
	v_exp_f16_sdwa v236, v236 dst_sel:WORD_0 dst_unused:UNUSED_PRESERVE src0_sel:WORD_0
	v_exp_f16_sdwa v237, v237 dst_sel:WORD_0 dst_unused:UNUSED_PRESERVE src0_sel:WORD_0
	v_exp_f16_sdwa v236, v236 dst_sel:WORD_1 dst_unused:UNUSED_PRESERVE src0_sel:WORD_1
	v_exp_f16_sdwa v237, v237 dst_sel:WORD_1 dst_unused:UNUSED_PRESERVE src0_sel:WORD_1
	v_pk_add_f16 v64, v239, v209
	v_pk_add_f16 v65, v240, v238
	v_pk_fma_f16 v236, v209, v236, v64 neg_lo:[1,0,0] neg_hi:[1,0,0]
	v_pk_fma_f16 v237, v238, v237, v65 neg_lo:[1,0,0] neg_hi:[1,0,0]
	s_nop 0
	v_cvt_pk_f16_f32 v209, v68, v69
	v_cvt_pk_f16_f32 v238, v70, v71
	v_and_b32 v66, s35, v209
	v_and_b32 v67, s35, v238
	v_pk_fma_f16 v64, v66, s42, v227
	v_pk_fma_f16 v65, v67, s42, v227
	v_pk_fma_f16 v64, v64, v66, s43
	v_pk_fma_f16 v65, v65, v67, s43
	s_nop 0
	v_pk_mul_f16 v64, v64, v66
	v_pk_mul_f16 v65, v65, v67
	v_exp_f16_sdwa v64, v64 dst_sel:WORD_0 dst_unused:UNUSED_PRESERVE src0_sel:WORD_0
	v_exp_f16_sdwa v65, v65 dst_sel:WORD_0 dst_unused:UNUSED_PRESERVE src0_sel:WORD_0
	v_exp_f16_sdwa v64, v64 dst_sel:WORD_1 dst_unused:UNUSED_PRESERVE src0_sel:WORD_1
	v_exp_f16_sdwa v65, v65 dst_sel:WORD_1 dst_unused:UNUSED_PRESERVE src0_sel:WORD_1
	v_pk_add_f16 v68, v209, v66
	v_pk_add_f16 v69, v238, v67
	v_pk_fma_f16 v64, v66, v64, v68 neg_lo:[1,0,0] neg_hi:[1,0,0]
	v_pk_fma_f16 v65, v67, v65, v69 neg_lo:[1,0,0] neg_hi:[1,0,0]
	s_nop 0
	v_cvt_pk_f16_f32 v70, v72, v73
	v_cvt_pk_f16_f32 v71, v74, v75
	v_and_b32 v68, s35, v70
	v_and_b32 v69, s35, v71
	v_pk_fma_f16 v66, v68, s42, v227
	v_pk_fma_f16 v67, v69, s42, v227
	v_pk_fma_f16 v66, v66, v68, s43
	v_pk_fma_f16 v67, v67, v69, s43
	s_nop 0
	v_pk_mul_f16 v66, v66, v68
	v_pk_mul_f16 v67, v67, v69
	v_exp_f16_sdwa v66, v66 dst_sel:WORD_0 dst_unused:UNUSED_PRESERVE src0_sel:WORD_0
	v_exp_f16_sdwa v67, v67 dst_sel:WORD_0 dst_unused:UNUSED_PRESERVE src0_sel:WORD_0
	v_exp_f16_sdwa v66, v66 dst_sel:WORD_1 dst_unused:UNUSED_PRESERVE src0_sel:WORD_1
	v_exp_f16_sdwa v67, v67 dst_sel:WORD_1 dst_unused:UNUSED_PRESERVE src0_sel:WORD_1
	v_pk_add_f16 v72, v70, v68
	v_pk_add_f16 v73, v71, v69
	v_pk_fma_f16 v66, v68, v66, v72 neg_lo:[1,0,0] neg_hi:[1,0,0]
	v_pk_fma_f16 v67, v69, v67, v73 neg_lo:[1,0,0] neg_hi:[1,0,0]
	s_nop 0
	v_cvt_pk_f16_f32 v72, v76, v77
	v_cvt_pk_f16_f32 v73, v78, v79
	v_and_b32 v70, s35, v72
	v_and_b32 v71, s35, v73
	v_pk_fma_f16 v68, v70, s42, v227
	v_pk_fma_f16 v69, v71, s42, v227
	v_pk_fma_f16 v68, v68, v70, s43
	v_pk_fma_f16 v69, v69, v71, s43
	s_nop 0
	v_pk_mul_f16 v68, v68, v70
	v_pk_mul_f16 v69, v69, v71
	v_exp_f16_sdwa v68, v68 dst_sel:WORD_0 dst_unused:UNUSED_PRESERVE src0_sel:WORD_0
	v_exp_f16_sdwa v69, v69 dst_sel:WORD_0 dst_unused:UNUSED_PRESERVE src0_sel:WORD_0
	v_exp_f16_sdwa v68, v68 dst_sel:WORD_1 dst_unused:UNUSED_PRESERVE src0_sel:WORD_1
	v_exp_f16_sdwa v69, v69 dst_sel:WORD_1 dst_unused:UNUSED_PRESERVE src0_sel:WORD_1
	v_pk_add_f16 v74, v72, v70
	v_pk_add_f16 v75, v73, v71
	v_pk_fma_f16 v68, v70, v68, v74 neg_lo:[1,0,0] neg_hi:[1,0,0]
	v_pk_fma_f16 v69, v71, v69, v75 neg_lo:[1,0,0] neg_hi:[1,0,0]
	s_nop 0
	v_cvt_pk_f16_f32 v74, v48, v49
	v_cvt_pk_f16_f32 v75, v50, v51
	v_and_b32 v72, s35, v74
	v_and_b32 v73, s35, v75
	v_pk_fma_f16 v70, v72, s42, v227
	v_pk_fma_f16 v71, v73, s42, v227
	v_pk_fma_f16 v70, v70, v72, s43
	v_pk_fma_f16 v71, v71, v73, s43
	s_nop 0
	v_pk_mul_f16 v70, v70, v72
	v_pk_mul_f16 v71, v71, v73
	v_exp_f16_sdwa v70, v70 dst_sel:WORD_0 dst_unused:UNUSED_PRESERVE src0_sel:WORD_0
	v_exp_f16_sdwa v71, v71 dst_sel:WORD_0 dst_unused:UNUSED_PRESERVE src0_sel:WORD_0
	v_exp_f16_sdwa v70, v70 dst_sel:WORD_1 dst_unused:UNUSED_PRESERVE src0_sel:WORD_1
	v_exp_f16_sdwa v71, v71 dst_sel:WORD_1 dst_unused:UNUSED_PRESERVE src0_sel:WORD_1
	v_pk_add_f16 v48, v74, v72
	v_pk_add_f16 v49, v75, v73
	v_pk_fma_f16 v70, v72, v70, v48 neg_lo:[1,0,0] neg_hi:[1,0,0]
	v_pk_fma_f16 v71, v73, v71, v49 neg_lo:[1,0,0] neg_hi:[1,0,0]
	s_nop 0
	v_cvt_pk_f16_f32 v72, v52, v53
	v_cvt_pk_f16_f32 v73, v54, v55
	v_and_b32 v50, s35, v72
	v_and_b32 v51, s35, v73
	v_pk_fma_f16 v48, v50, s42, v227
	v_pk_fma_f16 v49, v51, s42, v227
	v_pk_fma_f16 v48, v48, v50, s43
	v_pk_fma_f16 v49, v49, v51, s43
	s_nop 0
	v_pk_mul_f16 v48, v48, v50
	v_pk_mul_f16 v49, v49, v51
	v_exp_f16_sdwa v48, v48 dst_sel:WORD_0 dst_unused:UNUSED_PRESERVE src0_sel:WORD_0
	v_exp_f16_sdwa v49, v49 dst_sel:WORD_0 dst_unused:UNUSED_PRESERVE src0_sel:WORD_0
	v_exp_f16_sdwa v48, v48 dst_sel:WORD_1 dst_unused:UNUSED_PRESERVE src0_sel:WORD_1
	v_exp_f16_sdwa v49, v49 dst_sel:WORD_1 dst_unused:UNUSED_PRESERVE src0_sel:WORD_1
	v_pk_add_f16 v52, v72, v50
	v_pk_add_f16 v53, v73, v51
	v_pk_fma_f16 v48, v50, v48, v52 neg_lo:[1,0,0] neg_hi:[1,0,0]
	v_pk_fma_f16 v49, v51, v49, v53 neg_lo:[1,0,0] neg_hi:[1,0,0]
	s_nop 0
	v_cvt_pk_f16_f32 v54, v56, v57
	v_cvt_pk_f16_f32 v55, v58, v59
	v_and_b32 v52, s35, v54
	v_and_b32 v53, s35, v55
	v_pk_fma_f16 v50, v52, s42, v227
	v_pk_fma_f16 v51, v53, s42, v227
	v_pk_fma_f16 v50, v50, v52, s43
	v_pk_fma_f16 v51, v51, v53, s43
	s_nop 0
	v_pk_mul_f16 v50, v50, v52
	v_pk_mul_f16 v51, v51, v53
	v_exp_f16_sdwa v50, v50 dst_sel:WORD_0 dst_unused:UNUSED_PRESERVE src0_sel:WORD_0
	v_exp_f16_sdwa v51, v51 dst_sel:WORD_0 dst_unused:UNUSED_PRESERVE src0_sel:WORD_0
	v_exp_f16_sdwa v50, v50 dst_sel:WORD_1 dst_unused:UNUSED_PRESERVE src0_sel:WORD_1
	v_exp_f16_sdwa v51, v51 dst_sel:WORD_1 dst_unused:UNUSED_PRESERVE src0_sel:WORD_1
	v_pk_add_f16 v56, v54, v52
	v_pk_add_f16 v57, v55, v53
	v_pk_fma_f16 v50, v52, v50, v56 neg_lo:[1,0,0] neg_hi:[1,0,0]
	v_pk_fma_f16 v51, v53, v51, v57 neg_lo:[1,0,0] neg_hi:[1,0,0]
	s_nop 0
	v_cvt_pk_f16_f32 v56, v60, v61
	v_cvt_pk_f16_f32 v57, v62, v63
	v_and_b32 v54, s35, v56
	v_and_b32 v55, s35, v57
	v_pk_fma_f16 v52, v54, s42, v227
	v_pk_fma_f16 v53, v55, s42, v227
	v_pk_fma_f16 v52, v52, v54, s43
	v_pk_fma_f16 v53, v53, v55, s43
	s_nop 0
	v_pk_mul_f16 v52, v52, v54
	v_pk_mul_f16 v53, v53, v55
	v_exp_f16_sdwa v52, v52 dst_sel:WORD_0 dst_unused:UNUSED_PRESERVE src0_sel:WORD_0
	v_exp_f16_sdwa v53, v53 dst_sel:WORD_0 dst_unused:UNUSED_PRESERVE src0_sel:WORD_0
	v_exp_f16_sdwa v52, v52 dst_sel:WORD_1 dst_unused:UNUSED_PRESERVE src0_sel:WORD_1
	v_exp_f16_sdwa v53, v53 dst_sel:WORD_1 dst_unused:UNUSED_PRESERVE src0_sel:WORD_1
	v_pk_add_f16 v58, v56, v54
	v_pk_add_f16 v59, v57, v55
	v_pk_fma_f16 v52, v54, v52, v58 neg_lo:[1,0,0] neg_hi:[1,0,0]
	v_pk_fma_f16 v53, v55, v53, v59 neg_lo:[1,0,0] neg_hi:[1,0,0]
	ds_write2_b64 v228, v[236:237], v[70:71] offset0:78 offset1:142
	ds_write2st64_b64 v231, v[64:65], v[48:49] offset0:5 offset1:6
	ds_write2st64_b64 v232, v[66:67], v[50:51] offset0:9 offset1:10
	ds_write2st64_b64 v233, v[68:69], v[52:53] offset0:13 offset1:14
	v_cvt_pk_f16_f32 v52, v32, v33
	v_cvt_pk_f16_f32 v53, v34, v35
	v_and_b32 v50, s35, v52
	v_and_b32 v51, s35, v53
	v_pk_fma_f16 v48, v50, s42, v227
	v_pk_fma_f16 v49, v51, s42, v227
	v_pk_fma_f16 v48, v48, v50, s43
	v_pk_fma_f16 v49, v49, v51, s43
	v_mov_b32_e32 v237, 0xff800000
	v_pk_mul_f16 v48, v48, v50
	v_pk_mul_f16 v49, v49, v51
	v_exp_f16_sdwa v48, v48 dst_sel:WORD_0 dst_unused:UNUSED_PRESERVE src0_sel:WORD_0
	v_exp_f16_sdwa v49, v49 dst_sel:WORD_0 dst_unused:UNUSED_PRESERVE src0_sel:WORD_0
	v_exp_f16_sdwa v48, v48 dst_sel:WORD_1 dst_unused:UNUSED_PRESERVE src0_sel:WORD_1
	v_exp_f16_sdwa v49, v49 dst_sel:WORD_1 dst_unused:UNUSED_PRESERVE src0_sel:WORD_1
	v_pk_add_f16 v32, v52, v50
	v_pk_add_f16 v33, v53, v51
	v_pk_fma_f16 v48, v50, v48, v32 neg_lo:[1,0,0] neg_hi:[1,0,0]
	v_pk_fma_f16 v49, v51, v49, v33 neg_lo:[1,0,0] neg_hi:[1,0,0]
	v_mov_b32_e32 v236, 0
	v_cvt_pk_f16_f32 v50, v36, v37
	v_cvt_pk_f16_f32 v51, v38, v39
	v_and_b32 v34, s35, v50
	v_and_b32 v35, s35, v51
	v_pk_fma_f16 v32, v34, s42, v227
	v_pk_fma_f16 v33, v35, s42, v227
	v_pk_fma_f16 v32, v32, v34, s43
	v_pk_fma_f16 v33, v33, v35, s43
	s_nop 0
	v_pk_mul_f16 v32, v32, v34
	v_pk_mul_f16 v33, v33, v35
	v_exp_f16_sdwa v32, v32 dst_sel:WORD_0 dst_unused:UNUSED_PRESERVE src0_sel:WORD_0
	v_exp_f16_sdwa v33, v33 dst_sel:WORD_0 dst_unused:UNUSED_PRESERVE src0_sel:WORD_0
	v_exp_f16_sdwa v32, v32 dst_sel:WORD_1 dst_unused:UNUSED_PRESERVE src0_sel:WORD_1
	v_exp_f16_sdwa v33, v33 dst_sel:WORD_1 dst_unused:UNUSED_PRESERVE src0_sel:WORD_1
	v_pk_add_f16 v36, v50, v34
	v_pk_add_f16 v37, v51, v35
	v_pk_fma_f16 v32, v34, v32, v36 neg_lo:[1,0,0] neg_hi:[1,0,0]
	v_pk_fma_f16 v33, v35, v33, v37 neg_lo:[1,0,0] neg_hi:[1,0,0]
	s_nop 0
	v_cvt_pk_f16_f32 v38, v40, v41
	v_cvt_pk_f16_f32 v39, v42, v43
	v_and_b32 v36, s35, v38
	v_and_b32 v37, s35, v39
	v_pk_fma_f16 v34, v36, s42, v227
	v_pk_fma_f16 v35, v37, s42, v227
	v_pk_fma_f16 v34, v34, v36, s43
	v_pk_fma_f16 v35, v35, v37, s43
	s_nop 0
	v_pk_mul_f16 v34, v34, v36
	v_pk_mul_f16 v35, v35, v37
	v_exp_f16_sdwa v34, v34 dst_sel:WORD_0 dst_unused:UNUSED_PRESERVE src0_sel:WORD_0
	v_exp_f16_sdwa v35, v35 dst_sel:WORD_0 dst_unused:UNUSED_PRESERVE src0_sel:WORD_0
	v_exp_f16_sdwa v34, v34 dst_sel:WORD_1 dst_unused:UNUSED_PRESERVE src0_sel:WORD_1
	v_exp_f16_sdwa v35, v35 dst_sel:WORD_1 dst_unused:UNUSED_PRESERVE src0_sel:WORD_1
	v_pk_add_f16 v40, v38, v36
	v_pk_add_f16 v41, v39, v37
	v_pk_fma_f16 v34, v36, v34, v40 neg_lo:[1,0,0] neg_hi:[1,0,0]
	v_pk_fma_f16 v35, v37, v35, v41 neg_lo:[1,0,0] neg_hi:[1,0,0]
	s_nop 0
	v_cvt_pk_f16_f32 v40, v44, v45
	v_cvt_pk_f16_f32 v41, v46, v47
	v_and_b32 v38, s35, v40
	v_and_b32 v39, s35, v41
	v_pk_fma_f16 v36, v38, s42, v227
	v_pk_fma_f16 v37, v39, s42, v227
	v_pk_fma_f16 v36, v36, v38, s43
	v_pk_fma_f16 v37, v37, v39, s43
	s_nop 0
	v_pk_mul_f16 v36, v36, v38
	v_pk_mul_f16 v37, v37, v39
	v_exp_f16_sdwa v36, v36 dst_sel:WORD_0 dst_unused:UNUSED_PRESERVE src0_sel:WORD_0
	v_exp_f16_sdwa v37, v37 dst_sel:WORD_0 dst_unused:UNUSED_PRESERVE src0_sel:WORD_0
	v_exp_f16_sdwa v36, v36 dst_sel:WORD_1 dst_unused:UNUSED_PRESERVE src0_sel:WORD_1
	v_exp_f16_sdwa v37, v37 dst_sel:WORD_1 dst_unused:UNUSED_PRESERVE src0_sel:WORD_1
	v_pk_add_f16 v42, v40, v38
	v_pk_add_f16 v43, v41, v39
	v_pk_fma_f16 v36, v38, v36, v42 neg_lo:[1,0,0] neg_hi:[1,0,0]
	v_pk_fma_f16 v37, v39, v37, v43 neg_lo:[1,0,0] neg_hi:[1,0,0]
	s_nop 0
	v_cvt_pk_f16_f32 v42, v16, v17
	v_cvt_pk_f16_f32 v43, v18, v19
	v_and_b32 v40, s35, v42
	v_and_b32 v41, s35, v43
	v_pk_fma_f16 v38, v40, s42, v227
	v_pk_fma_f16 v39, v41, s42, v227
	v_pk_fma_f16 v38, v38, v40, s43
	v_pk_fma_f16 v39, v39, v41, s43
	s_nop 0
	v_pk_mul_f16 v38, v38, v40
	v_pk_mul_f16 v39, v39, v41
	v_exp_f16_sdwa v38, v38 dst_sel:WORD_0 dst_unused:UNUSED_PRESERVE src0_sel:WORD_0
	v_exp_f16_sdwa v39, v39 dst_sel:WORD_0 dst_unused:UNUSED_PRESERVE src0_sel:WORD_0
	v_exp_f16_sdwa v38, v38 dst_sel:WORD_1 dst_unused:UNUSED_PRESERVE src0_sel:WORD_1
	v_exp_f16_sdwa v39, v39 dst_sel:WORD_1 dst_unused:UNUSED_PRESERVE src0_sel:WORD_1
	v_pk_add_f16 v16, v42, v40
	v_pk_add_f16 v17, v43, v41
	v_pk_fma_f16 v38, v40, v38, v16 neg_lo:[1,0,0] neg_hi:[1,0,0]
	v_pk_fma_f16 v39, v41, v39, v17 neg_lo:[1,0,0] neg_hi:[1,0,0]
	s_nop 0
	v_cvt_pk_f16_f32 v40, v20, v21
	v_cvt_pk_f16_f32 v41, v22, v23
	v_and_b32 v18, s35, v40
	v_and_b32 v19, s35, v41
	v_pk_fma_f16 v16, v18, s42, v227
	v_pk_fma_f16 v17, v19, s42, v227
	v_pk_fma_f16 v16, v16, v18, s43
	v_pk_fma_f16 v17, v17, v19, s43
	s_nop 0
	v_pk_mul_f16 v16, v16, v18
	v_pk_mul_f16 v17, v17, v19
	v_exp_f16_sdwa v16, v16 dst_sel:WORD_0 dst_unused:UNUSED_PRESERVE src0_sel:WORD_0
	v_exp_f16_sdwa v17, v17 dst_sel:WORD_0 dst_unused:UNUSED_PRESERVE src0_sel:WORD_0
	v_exp_f16_sdwa v16, v16 dst_sel:WORD_1 dst_unused:UNUSED_PRESERVE src0_sel:WORD_1
	v_exp_f16_sdwa v17, v17 dst_sel:WORD_1 dst_unused:UNUSED_PRESERVE src0_sel:WORD_1
	v_pk_add_f16 v20, v40, v18
	v_pk_add_f16 v21, v41, v19
	v_pk_fma_f16 v16, v18, v16, v20 neg_lo:[1,0,0] neg_hi:[1,0,0]
	v_pk_fma_f16 v17, v19, v17, v21 neg_lo:[1,0,0] neg_hi:[1,0,0]
	s_nop 0
	v_cvt_pk_f16_f32 v22, v24, v25
	v_cvt_pk_f16_f32 v23, v26, v27
	v_and_b32 v20, s35, v22
	v_and_b32 v21, s35, v23
	v_pk_fma_f16 v18, v20, s42, v227
	v_pk_fma_f16 v19, v21, s42, v227
	v_pk_fma_f16 v18, v18, v20, s43
	v_pk_fma_f16 v19, v19, v21, s43
	s_nop 0
	v_pk_mul_f16 v18, v18, v20
	v_pk_mul_f16 v19, v19, v21
	v_exp_f16_sdwa v18, v18 dst_sel:WORD_0 dst_unused:UNUSED_PRESERVE src0_sel:WORD_0
	v_exp_f16_sdwa v19, v19 dst_sel:WORD_0 dst_unused:UNUSED_PRESERVE src0_sel:WORD_0
	v_exp_f16_sdwa v18, v18 dst_sel:WORD_1 dst_unused:UNUSED_PRESERVE src0_sel:WORD_1
	v_exp_f16_sdwa v19, v19 dst_sel:WORD_1 dst_unused:UNUSED_PRESERVE src0_sel:WORD_1
	v_pk_add_f16 v24, v22, v20
	v_pk_add_f16 v25, v23, v21
	v_pk_fma_f16 v18, v20, v18, v24 neg_lo:[1,0,0] neg_hi:[1,0,0]
	v_pk_fma_f16 v19, v21, v19, v25 neg_lo:[1,0,0] neg_hi:[1,0,0]
	s_nop 0
	v_cvt_pk_f16_f32 v24, v28, v29
	v_cvt_pk_f16_f32 v25, v30, v31
	v_and_b32 v22, s35, v24
	v_and_b32 v23, s35, v25
	v_pk_fma_f16 v20, v22, s42, v227
	v_pk_fma_f16 v21, v23, s42, v227
	v_pk_fma_f16 v20, v20, v22, s43
	v_pk_fma_f16 v21, v21, v23, s43
	s_nop 0
	v_pk_mul_f16 v20, v20, v22
	v_pk_mul_f16 v21, v21, v23
	v_exp_f16_sdwa v20, v20 dst_sel:WORD_0 dst_unused:UNUSED_PRESERVE src0_sel:WORD_0
	v_exp_f16_sdwa v21, v21 dst_sel:WORD_0 dst_unused:UNUSED_PRESERVE src0_sel:WORD_0
	v_exp_f16_sdwa v20, v20 dst_sel:WORD_1 dst_unused:UNUSED_PRESERVE src0_sel:WORD_1
	v_exp_f16_sdwa v21, v21 dst_sel:WORD_1 dst_unused:UNUSED_PRESERVE src0_sel:WORD_1
	v_pk_add_f16 v26, v24, v22
	v_pk_add_f16 v27, v25, v23
	v_pk_fma_f16 v20, v22, v20, v26 neg_lo:[1,0,0] neg_hi:[1,0,0]
	v_pk_fma_f16 v21, v23, v21, v27 neg_lo:[1,0,0] neg_hi:[1,0,0]
	ds_write2st64_b64 v234, v[48:49], v[38:39] offset0:3 offset1:4
	ds_write2st64_b64 v231, v[32:33], v[16:17] offset0:7 offset1:8
	ds_write2st64_b64 v232, v[34:35], v[18:19] offset0:11 offset1:12
	ds_write2st64_b64 v233, v[36:37], v[20:21] offset0:15 offset1:16
	s_mul_i32 s0, s3, 0x280
	v_add_u32_e32 v44, s0, v248
	ds_read_b128 v[16:19], v44
	ds_read_b128 v[20:23], v44 offset:64
	v_mov_b32_e32 v252, 0
	v_mov_b32_e32 v253, 0
	v_mov_b32_e32 v254, 0
	v_mov_b32_e32 v255, 0
	s_waitcnt vmcnt(2)
	s_branch .LBB0_25
.LBB0_23:
	v_mov_b32_e32 v237, v48
	v_sub_f32_e32 v252, 0, v48
	v_sub_f32_e32 v253, 0, v48
	v_sub_f32_e32 v254, 0, v48
	v_sub_f32_e32 v255, 0, v48
.LBB0_24:
	v_sub_f32_e32 v24, v32, v48
	v_exp_f32_e32 v24, v24
	v_sub_f32_e32 v25, v33, v48
	v_exp_f32_e32 v25, v25
	v_sub_f32_e32 v26, v34, v48
	v_exp_f32_e32 v26, v26
	v_sub_f32_e32 v27, v35, v48
	v_exp_f32_e32 v27, v27
	v_sub_f32_e32 v28, v36, v48
	v_exp_f32_e32 v28, v28
	v_sub_f32_e32 v29, v37, v48
	v_exp_f32_e32 v29, v29
	v_sub_f32_e32 v30, v38, v48
	v_exp_f32_e32 v30, v30
	v_sub_f32_e32 v31, v39, v48
	v_exp_f32_e32 v31, v31
	s_branch .Lsm_tail
.Lsm_nosub:
	v_exp_f32_e32 v24, v32
	v_exp_f32_e32 v25, v33
	v_exp_f32_e32 v26, v34
	v_exp_f32_e32 v27, v35
	v_exp_f32_e32 v28, v36
	v_exp_f32_e32 v29, v37
	v_exp_f32_e32 v30, v38
	v_exp_f32_e32 v31, v39
.Lsm_tail:
	ds_read_b64_tr_b16 v[48:49], v251
	ds_read_b64_tr_b16 v[50:51], v251 offset:2176
	ds_read_b64_tr_b16 v[52:53], v251 offset:32
	ds_read_b64_tr_b16 v[54:55], v251 offset:2208
	ds_read_b64_tr_b16 v[56:57], v251 offset:64
	ds_read_b64_tr_b16 v[58:59], v251 offset:2240
	ds_read_b64_tr_b16 v[60:61], v251 offset:96
	ds_read_b64_tr_b16 v[62:63], v251 offset:2272
	v_cvt_pk_f16_f32 v40, v24, v25
	v_cvt_pk_f16_f32 v41, v26, v27
	v_cvt_pk_f16_f32 v42, v28, v29
	v_cvt_pk_f16_f32 v43, v30, v31
	v_dot2c_f32_f16_e32 v236, 0x3c003c00, v40
	v_dot2c_f32_f16_e32 v236, 0x3c003c00, v41
	v_dot2c_f32_f16_e32 v236, 0x3c003c00, v42
	v_dot2c_f32_f16_e32 v236, 0x3c003c00, v43
	s_waitcnt lgkmcnt(6)
	v_mfma_f32_16x16x32_f16 v[0:3], v[48:51], v[40:43], v[0:3]
	s_waitcnt lgkmcnt(4)
	v_mfma_f32_16x16x32_f16 v[4:7], v[52:55], v[40:43], v[4:7]
	s_addk_i32 s8, 0x200
	s_waitcnt lgkmcnt(2)
	v_mfma_f32_16x16x32_f16 v[8:11], v[56:59], v[40:43], v[8:11]
	s_cmpk_eq_i32 s8, 0x800
	s_waitcnt lgkmcnt(0)
	v_mfma_f32_16x16x32_f16 v[12:15], v[60:63], v[40:43], v[12:15]
	s_cbranch_scc1 .LBB0_28

.Lno_pre:
	s_nop 15
	s_nop 3
	v_cvt_pk_f16_f32 v38, v64, v65
	v_cvt_pk_f16_f32 v39, v66, v67
	v_and_b32 v36, s35, v38
	v_and_b32 v37, s35, v39
	v_pk_fma_f16 v238, v36, s42, v227
	v_pk_fma_f16 v239, v37, s42, v227
	v_pk_fma_f16 v238, v238, v36, s43
	v_pk_fma_f16 v239, v239, v37, s43
	s_nop 0
	v_pk_mul_f16 v238, v238, v36
	v_pk_mul_f16 v239, v239, v37
	v_exp_f16_sdwa v238, v238 dst_sel:WORD_0 dst_unused:UNUSED_PRESERVE src0_sel:WORD_0
	v_exp_f16_sdwa v239, v239 dst_sel:WORD_0 dst_unused:UNUSED_PRESERVE src0_sel:WORD_0
	v_exp_f16_sdwa v238, v238 dst_sel:WORD_1 dst_unused:UNUSED_PRESERVE src0_sel:WORD_1
	v_exp_f16_sdwa v239, v239 dst_sel:WORD_1 dst_unused:UNUSED_PRESERVE src0_sel:WORD_1
	v_pk_add_f16 v40, v38, v36
	v_pk_add_f16 v41, v39, v37
	v_pk_fma_f16 v238, v36, v238, v40 neg_lo:[1,0,0] neg_hi:[1,0,0]
	v_pk_fma_f16 v239, v37, v239, v41 neg_lo:[1,0,0] neg_hi:[1,0,0]
	v_cvt_pk_f16_f32 v38, v68, v69
	v_cvt_pk_f16_f32 v39, v70, v71
	v_and_b32 v36, s35, v38
	v_and_b32 v37, s35, v39
	v_pk_fma_f16 v240, v36, s42, v227
	v_pk_fma_f16 v241, v37, s42, v227
	v_pk_fma_f16 v240, v240, v36, s43
	v_pk_fma_f16 v241, v241, v37, s43
	v_cvt_pk_f16_f32 v243, v72, v73
	v_cvt_pk_f16_f32 v244, v74, v75
	v_and_b32 v209, s35, v243
	v_and_b32 v242, s35, v244
	v_pk_fma_f16 v68, v209, s42, v227
	v_pk_fma_f16 v69, v242, s42, v227
	v_pk_fma_f16 v68, v68, v209, s43
	v_pk_fma_f16 v69, v69, v242, s43
	v_cvt_pk_f16_f32 v74, v76, v77
	v_cvt_pk_f16_f32 v75, v78, v79
	v_and_b32 v72, s35, v74
	v_and_b32 v73, s35, v75
	v_pk_fma_f16 v70, v72, s42, v227
	v_pk_fma_f16 v71, v73, s42, v227
	v_pk_fma_f16 v70, v70, v72, s43
	v_pk_fma_f16 v71, v71, v73, s43
	s_cmp_eq_u32 s8, 0
	v_pk_mul_f16 v240, v240, v36
	v_pk_mul_f16 v241, v241, v37
	v_exp_f16_sdwa v240, v240 dst_sel:WORD_0 dst_unused:UNUSED_PRESERVE src0_sel:WORD_0
	v_exp_f16_sdwa v241, v241 dst_sel:WORD_0 dst_unused:UNUSED_PRESERVE src0_sel:WORD_0
	v_exp_f16_sdwa v240, v240 dst_sel:WORD_1 dst_unused:UNUSED_PRESERVE src0_sel:WORD_1
	v_exp_f16_sdwa v241, v241 dst_sel:WORD_1 dst_unused:UNUSED_PRESERVE src0_sel:WORD_1
	v_pk_add_f16 v40, v38, v36
	v_pk_add_f16 v41, v39, v37
	v_pk_fma_f16 v240, v36, v240, v40 neg_lo:[1,0,0] neg_hi:[1,0,0]
	v_pk_fma_f16 v241, v37, v241, v41 neg_lo:[1,0,0] neg_hi:[1,0,0]
	v_pk_mul_f16 v68, v68, v209
	v_pk_mul_f16 v69, v69, v242
	v_exp_f16_sdwa v68, v68 dst_sel:WORD_0 dst_unused:UNUSED_PRESERVE src0_sel:WORD_0
	v_exp_f16_sdwa v69, v69 dst_sel:WORD_0 dst_unused:UNUSED_PRESERVE src0_sel:WORD_0
	v_exp_f16_sdwa v68, v68 dst_sel:WORD_1 dst_unused:UNUSED_PRESERVE src0_sel:WORD_1
	v_exp_f16_sdwa v69, v69 dst_sel:WORD_1 dst_unused:UNUSED_PRESERVE src0_sel:WORD_1
	v_pk_add_f16 v76, v243, v209
	v_pk_add_f16 v77, v244, v242
	v_pk_fma_f16 v68, v209, v68, v76 neg_lo:[1,0,0] neg_hi:[1,0,0]
	v_pk_fma_f16 v69, v242, v69, v77 neg_lo:[1,0,0] neg_hi:[1,0,0]
	v_pk_mul_f16 v70, v70, v72
	v_pk_mul_f16 v71, v71, v73
	v_exp_f16_sdwa v70, v70 dst_sel:WORD_0 dst_unused:UNUSED_PRESERVE src0_sel:WORD_0
	v_exp_f16_sdwa v71, v71 dst_sel:WORD_0 dst_unused:UNUSED_PRESERVE src0_sel:WORD_0
	v_exp_f16_sdwa v70, v70 dst_sel:WORD_1 dst_unused:UNUSED_PRESERVE src0_sel:WORD_1
	v_exp_f16_sdwa v71, v71 dst_sel:WORD_1 dst_unused:UNUSED_PRESERVE src0_sel:WORD_1
	v_pk_add_f16 v76, v74, v72
	v_pk_add_f16 v77, v75, v73
	v_pk_fma_f16 v70, v72, v70, v76 neg_lo:[1,0,0] neg_hi:[1,0,0]
	v_pk_fma_f16 v71, v73, v71, v77 neg_lo:[1,0,0] neg_hi:[1,0,0]
	v_cvt_pk_f16_f32 v74, v48, v49
	v_cvt_pk_f16_f32 v75, v50, v51
	v_and_b32 v72, s35, v74
	v_and_b32 v73, s35, v75
	v_pk_fma_f16 v64, v72, s42, v227
	v_pk_fma_f16 v65, v73, s42, v227
	v_pk_fma_f16 v64, v64, v72, s43
	v_pk_fma_f16 v65, v65, v73, s43
	v_cvt_pk_f16_f32 v78, v52, v53
	v_cvt_pk_f16_f32 v79, v54, v55
	v_and_b32 v76, s35, v78
	v_and_b32 v77, s35, v79
	v_pk_fma_f16 v66, v76, s42, v227
	v_pk_fma_f16 v67, v77, s42, v227
	v_pk_fma_f16 v66, v66, v76, s43
	v_pk_fma_f16 v67, v67, v77, s43
	v_pk_mul_f16 v64, v64, v72
	v_pk_mul_f16 v65, v65, v73
	v_exp_f16_sdwa v64, v64 dst_sel:WORD_0 dst_unused:UNUSED_PRESERVE src0_sel:WORD_0
	v_exp_f16_sdwa v65, v65 dst_sel:WORD_0 dst_unused:UNUSED_PRESERVE src0_sel:WORD_0
	v_exp_f16_sdwa v64, v64 dst_sel:WORD_1 dst_unused:UNUSED_PRESERVE src0_sel:WORD_1
	v_exp_f16_sdwa v65, v65 dst_sel:WORD_1 dst_unused:UNUSED_PRESERVE src0_sel:WORD_1
	v_pk_add_f16 v209, v74, v72
	v_pk_add_f16 v242, v75, v73
	v_pk_fma_f16 v64, v72, v64, v209 neg_lo:[1,0,0] neg_hi:[1,0,0]
	v_pk_fma_f16 v65, v73, v65, v242 neg_lo:[1,0,0] neg_hi:[1,0,0]
	v_pk_mul_f16 v66, v66, v76
	v_pk_mul_f16 v67, v67, v77
	v_exp_f16_sdwa v66, v66 dst_sel:WORD_0 dst_unused:UNUSED_PRESERVE src0_sel:WORD_0
	v_exp_f16_sdwa v67, v67 dst_sel:WORD_0 dst_unused:UNUSED_PRESERVE src0_sel:WORD_0
	v_exp_f16_sdwa v66, v66 dst_sel:WORD_1 dst_unused:UNUSED_PRESERVE src0_sel:WORD_1
	v_exp_f16_sdwa v67, v67 dst_sel:WORD_1 dst_unused:UNUSED_PRESERVE src0_sel:WORD_1
	v_pk_add_f16 v72, v78, v76
	v_pk_add_f16 v73, v79, v77
	v_pk_fma_f16 v66, v76, v66, v72 neg_lo:[1,0,0] neg_hi:[1,0,0]
	v_pk_fma_f16 v67, v77, v67, v73 neg_lo:[1,0,0] neg_hi:[1,0,0]
	v_cvt_pk_f16_f32 v74, v56, v57
	v_cvt_pk_f16_f32 v75, v58, v59
	v_and_b32 v72, s35, v74
	v_and_b32 v73, s35, v75
	v_pk_fma_f16 v48, v72, s42, v227
	v_pk_fma_f16 v49, v73, s42, v227
	v_pk_fma_f16 v48, v48, v72, s43
	v_pk_fma_f16 v49, v49, v73, s43
	v_cvt_pk_f16_f32 v58, v60, v61
	v_cvt_pk_f16_f32 v59, v62, v63
	v_and_b32 v56, s35, v58
	v_and_b32 v57, s35, v59
	v_pk_fma_f16 v50, v56, s42, v227
	v_pk_fma_f16 v51, v57, s42, v227
	v_pk_fma_f16 v50, v50, v56, s43
	v_pk_fma_f16 v51, v51, v57, s43
	v_pk_mul_f16 v48, v48, v72
	v_pk_mul_f16 v49, v49, v73
	v_exp_f16_sdwa v48, v48 dst_sel:WORD_0 dst_unused:UNUSED_PRESERVE src0_sel:WORD_0
	v_exp_f16_sdwa v49, v49 dst_sel:WORD_0 dst_unused:UNUSED_PRESERVE src0_sel:WORD_0
	v_exp_f16_sdwa v48, v48 dst_sel:WORD_1 dst_unused:UNUSED_PRESERVE src0_sel:WORD_1
	v_exp_f16_sdwa v49, v49 dst_sel:WORD_1 dst_unused:UNUSED_PRESERVE src0_sel:WORD_1
	v_pk_add_f16 v62, v74, v72
	v_pk_add_f16 v63, v75, v73
	v_pk_fma_f16 v48, v72, v48, v62 neg_lo:[1,0,0] neg_hi:[1,0,0]
	v_pk_fma_f16 v49, v73, v49, v63 neg_lo:[1,0,0] neg_hi:[1,0,0]
	v_pk_mul_f16 v50, v50, v56
	v_pk_mul_f16 v51, v51, v57
	v_exp_f16_sdwa v50, v50 dst_sel:WORD_0 dst_unused:UNUSED_PRESERVE src0_sel:WORD_0
	v_exp_f16_sdwa v51, v51 dst_sel:WORD_0 dst_unused:UNUSED_PRESERVE src0_sel:WORD_0
	v_exp_f16_sdwa v50, v50 dst_sel:WORD_1 dst_unused:UNUSED_PRESERVE src0_sel:WORD_1
	v_exp_f16_sdwa v51, v51 dst_sel:WORD_1 dst_unused:UNUSED_PRESERVE src0_sel:WORD_1
	v_pk_add_f16 v62, v58, v56
	v_pk_add_f16 v63, v59, v57
	v_pk_fma_f16 v50, v56, v50, v62 neg_lo:[1,0,0] neg_hi:[1,0,0]
	v_pk_fma_f16 v51, v57, v51, v63 neg_lo:[1,0,0] neg_hi:[1,0,0]
	ds_write2_b64 v246, v[238:239], v[240:241] offset0:136 offset1:138
	ds_write2_b64 v246, v[64:65], v[66:67] offset0:144 offset1:146
	ds_write2_b64 v246, v[68:69], v[70:71] offset0:140 offset1:142
	ds_write2_b64 v246, v[48:49], v[50:51] offset0:148 offset1:150
	ds_read2_b64 v[24:27], v249 offset1:1
	ds_read2_b64 v[28:31], v249 offset0:8 offset1:9
	ds_read2_b64 v[40:43], v250 offset1:1
	ds_read2_b64 v[44:47], v250 offset0:8 offset1:9
	s_waitcnt lgkmcnt(2)
	v_mfma_f32_16x16x32_f16 v[32:35], v[24:27], v[16:19], v[252:255]
	v_mfma_f32_16x16x32_f16 v[32:35], v[28:31], v[20:23], v[32:35]
	s_waitcnt lgkmcnt(0)
	v_mfma_f32_16x16x32_f16 v[36:39], v[40:43], v[16:19], v[252:255]
	v_mfma_f32_16x16x32_f16 v[36:39], v[44:47], v[20:23], v[36:39]
	s_nop 7
	v_max3_f32 v52, v32, v33, v34
	v_max3_f32 v52, v52, v35, v36
	v_max3_f32 v52, v52, v37, v38
	v_max_f32_e32 v52, v52, v39
	v_mov_b32_e32 v53, v52
	s_nop 1
	v_permlane16_swap_b32_e32 v52, v53
	s_nop 0
	v_max_f32_e32 v52, v52, v53
	v_mov_b32_e32 v53, v52
	s_nop 1
	v_permlane32_swap_b32_e32 v52, v53
	s_nop 0
	v_max_f32_e32 v48, v52, v53
	s_cbranch_scc1 .LBB0_23
	v_cmp_lt_f32_e32 vcc, 0x41000000, v48
	s_cbranch_vccz .Lsm_nosub
	v_add_f32_e32 v237, v237, v48
	v_sub_f32_e32 v52, 0, v48
	v_exp_f32_e32 v52, v52
	v_sub_f32_e32 v252, 0, v237
	v_sub_f32_e32 v253, 0, v237
	v_sub_f32_e32 v254, 0, v237
	v_sub_f32_e32 v255, 0, v237
	v_pk_mul_f32 v[14:15], v[52:53], v[14:15] op_sel_hi:[0,1]
	v_pk_mul_f32 v[12:13], v[52:53], v[12:13] op_sel_hi:[0,1]
	v_pk_mul_f32 v[10:11], v[52:53], v[10:11] op_sel_hi:[0,1]
	v_pk_mul_f32 v[8:9], v[52:53], v[8:9] op_sel_hi:[0,1]
	v_pk_mul_f32 v[6:7], v[52:53], v[6:7] op_sel_hi:[0,1]
	v_pk_mul_f32 v[4:5], v[52:53], v[4:5] op_sel_hi:[0,1]
	v_pk_mul_f32 v[2:3], v[52:53], v[2:3] op_sel_hi:[0,1]
	v_pk_mul_f32 v[0:1], v[52:53], v[0:1] op_sel_hi:[0,1]
	v_mul_f32_e32 v236, v236, v52
	s_branch .LBB0_24
.LBB0_28:
	ds_bpermute_b32 v32, v247, v236
	v_and_b32_e32 v40, 15, v215
	s_waitcnt lgkmcnt(0)
	v_add_f32_e32 v41, v236, v32
	s_nop 0
	ds_bpermute_b32 v32, v245, v41
	v_cmp_gt_u32_e32 vcc, 5, v40
	s_nop 1
	s_and_saveexec_b64 s[0:1], vcc
	s_cbranch_execz .LBB0_21
	s_waitcnt lgkmcnt(0)
	v_add_f32_e32 v32, v41, v32
	v_div_scale_f32 v33, s[10:11], v32, v32, 0.5
	v_rcp_f32_e32 v34, v33
	v_div_scale_f32 v35, vcc, 0.5, v32, 0.5
	v_fma_f32 v36, -v33, v34, 1.0
	v_fmac_f32_e32 v34, v36, v34
	v_mul_f32_e32 v36, v35, v34
	v_fma_f32 v37, -v33, v36, v35
	v_fmac_f32_e32 v36, v37, v34
	v_fma_f32 v33, -v33, v36, v35
	v_div_fmas_f32 v33, v33, v34, v36
	v_div_fixup_f32 v32, v33, v32, 0.5
	v_add_u32_e32 v33, s3, v221
	v_mov_b32_e32 v34, v40
	v_mad_u64_u32 v[34:35], s[8:9], v33, 5, v[34:35]
	v_sub_u32_e32 v36, v222, v214
	v_lshrrev_b32_e32 v37, 4, v215
	v_lshl_add_u32 v36, v37, 3, v36
	v_lshl_add_u32 v33, v34, 7, v36
	v_pk_mul_f32 v[44:45], v[32:33], v[0:1] op_sel_hi:[0,1]
	v_pk_mul_f32 v[46:47], v[32:33], v[2:3] op_sel_hi:[0,1]
	v_cvt_pk_f16_f32 v44, v44, v45
	v_cvt_pk_f16_f32 v45, v46, v47
	ds_write_b64 v33, v[44:45]
	v_pk_mul_f32 v[48:49], v[32:33], v[4:5] op_sel_hi:[0,1]
	v_pk_mul_f32 v[50:51], v[32:33], v[6:7] op_sel_hi:[0,1]
	v_cvt_pk_f16_f32 v48, v48, v49
	v_cvt_pk_f16_f32 v49, v50, v51
	ds_write_b64 v33, v[48:49] offset:32
	v_pk_mul_f32 v[52:53], v[32:33], v[8:9] op_sel_hi:[0,1]
	v_pk_mul_f32 v[54:55], v[32:33], v[10:11] op_sel_hi:[0,1]
	v_cvt_pk_f16_f32 v52, v52, v53
	v_cvt_pk_f16_f32 v53, v54, v55
	ds_write_b64 v33, v[52:53] offset:64
	v_pk_mul_f32 v[56:57], v[32:33], v[12:13] op_sel_hi:[0,1]
	v_pk_mul_f32 v[58:59], v[32:33], v[14:15] op_sel_hi:[0,1]
	v_cvt_pk_f16_f32 v56, v56, v57
	v_cvt_pk_f16_f32 v57, v58, v59
	ds_write_b64 v33, v[56:57] offset:96
	s_branch .LBB0_21
